# speedup vs baseline: 1.0136x; 1.0026x over previous
_Z7gemm128ILi3ELi96EEv8GemmArgs:
	s_cmp_ge_u32 s2, 0x100
	s_cbranch_scc1 .Ldn_exit
	s_load_dwordx4 s[4:7], s[0:1], 0x0
	s_load_dwordx2 s[8:9], s[0:1], 0x20
	s_load_dwordx2 s[10:11], s[0:1], 0x38
	s_and_b32 s12, s2, 7
	s_lshr_b32 s13, s2, 3
	s_lshl_b32 s12, s12, 5
	s_add_u32 s12, s12, s13
	s_and_b32 s13, s12, 3
	s_lshr_b32 s12, s12, 2
	s_lshl_b32 s12, s12, 7
	s_mul_i32 s13, s13, 0xc0
	v_lshrrev_b32_e32 v1, 6, v0
	v_and_b32_e32 v14, 7, v0
	v_bfe_u32 v15, v0, 4, 3
	v_xor_b32_e32 v14, v14, v15
	v_readfirstlane_b32 s14, v1
	v_lshrrev_b32_e32 v15, 3, v0
	v_mul_u32_u24_e32 v15, 0x1800, v15
	v_lshl_add_u32 v2, v14, 4, v15
	s_mov_b32 s22, 0x30000
	v_add_u32_e32 v3, s22, v2
	v_add_u32_e32 v4, s22, v3
	v_add_u32_e32 v5, s22, v4
	v_add_u32_e32 v6, s22, v5
	v_add_u32_e32 v7, s22, v6
	v_and_b32_e32 v14, 15, v0
	v_bfe_u32 v15, v0, 4, 2
	v_lshrrev_b32_e32 v16, 1, v14
	v_xor_b32_e32 v16, v16, v15
	v_lshlrev_b32_e32 v16, 4, v16
	v_bfe_u32 v17, v0, 7, 1
	v_bfe_u32 v18, v0, 6, 1
	v_lshl_add_u32 v19, v17, 6, v14
	v_lshl_add_u32 v8, v19, 7, v16
	v_mul_u32_u24_e32 v19, 0x60, v18
	v_add_u32_e32 v19, v19, v14
	v_lshl_add_u32 v9, v19, 7, v16
	v_add_u32_e32 v9, 0x4000, v9
	v_lshl_add_u32 v19, v17, 6, v14
	v_add_u32_e32 v19, s12, v19
	v_mul_u32_u24_e32 v19, 0xc00, v19
	v_mul_u32_u24_e32 v60, 0x60, v18
	v_lshl_add_u32 v60, v15, 2, v60
	v_add_u32_e32 v60, s13, v60
	v_lshl_add_u32 v56, v60, 2, v19
	s_mov_b32 s22, 0xc000
	v_add_u32_e32 v57, s22, v56
	v_add_u32_e32 v58, s22, v57
	v_add_u32_e32 v59, s22, v58
	s_waitcnt lgkmcnt(0)
	s_mul_i32 s22, s12, 0x1800
	s_add_u32 s16, s4, s22
	s_addc_u32 s17, s5, 0
	s_mul_i32 s22, s13, 0x1800
	s_add_u32 s18, s6, s22
	s_addc_u32 s19, s7, 0
	s_lshl_b32 s20, s14, 10
	s_mov_b32 s21, 0
	s_add_u32 m0, s20, 0x0
	s_nop 0
	global_load_lds_dwordx4 v2, s[16:17]
	s_add_u32 m0, s20, 0x1000
	s_nop 0
	global_load_lds_dwordx4 v3, s[16:17]
	s_add_u32 m0, s20, 0x2000
	s_nop 0
	global_load_lds_dwordx4 v4, s[16:17]
	s_add_u32 m0, s20, 0x3000
	s_nop 0
	global_load_lds_dwordx4 v5, s[16:17]
	s_add_u32 m0, s20, 0x4000
	s_nop 0
	global_load_lds_dwordx4 v2, s[18:19]
	s_add_u32 m0, s20, 0x5000
	s_nop 0
	global_load_lds_dwordx4 v3, s[18:19]
	s_add_u32 m0, s20, 0x6000
	s_nop 0
	global_load_lds_dwordx4 v4, s[18:19]
	s_add_u32 m0, s20, 0x7000
	s_nop 0
	global_load_lds_dwordx4 v5, s[18:19]
	s_add_u32 m0, s20, 0x8000
	s_nop 0
	global_load_lds_dwordx4 v6, s[18:19]
	s_add_u32 m0, s20, 0x9000
	s_nop 0
	global_load_lds_dwordx4 v7, s[18:19]
	s_add_u32 s16, s16, 0x80
	s_addc_u32 s17, s17, 0
	s_add_u32 s18, s18, 0x80
	s_addc_u32 s19, s19, 0
	s_add_u32 s20, s20, 0xa000
	s_sub_u32 s22, s20, 0x28000
	s_cmp_ge_u32 s20, 0x28000
	s_cselect_b32 s20, s22, s20
	s_add_u32 m0, s20, 0x0
	s_nop 0
	global_load_lds_dwordx4 v2, s[16:17]
	s_add_u32 m0, s20, 0x1000
	s_nop 0
	global_load_lds_dwordx4 v3, s[16:17]
	s_add_u32 m0, s20, 0x2000
	s_nop 0
	global_load_lds_dwordx4 v4, s[16:17]
	s_add_u32 m0, s20, 0x3000
	s_nop 0
	global_load_lds_dwordx4 v5, s[16:17]
	s_add_u32 m0, s20, 0x4000
	s_nop 0
	global_load_lds_dwordx4 v2, s[18:19]
	s_add_u32 m0, s20, 0x5000
	s_nop 0
	global_load_lds_dwordx4 v3, s[18:19]
	s_add_u32 m0, s20, 0x6000
	s_nop 0
	global_load_lds_dwordx4 v4, s[18:19]
	s_add_u32 m0, s20, 0x7000
	s_nop 0
	global_load_lds_dwordx4 v5, s[18:19]
	s_add_u32 m0, s20, 0x8000
	s_nop 0
	global_load_lds_dwordx4 v6, s[18:19]
	s_add_u32 m0, s20, 0x9000
	s_nop 0
	global_load_lds_dwordx4 v7, s[18:19]
	s_add_u32 s16, s16, 0x80
	s_addc_u32 s17, s17, 0
	s_add_u32 s18, s18, 0x80
	s_addc_u32 s19, s19, 0
	s_add_u32 s20, s20, 0xa000
	s_sub_u32 s22, s20, 0x28000
	s_cmp_ge_u32 s20, 0x28000
	s_cselect_b32 s20, s22, s20
	s_add_u32 m0, s20, 0x0
	s_nop 0
	global_load_lds_dwordx4 v2, s[16:17]
	s_add_u32 m0, s20, 0x1000
	s_nop 0
	global_load_lds_dwordx4 v3, s[16:17]
	s_add_u32 m0, s20, 0x2000
	s_nop 0
	global_load_lds_dwordx4 v4, s[16:17]
	s_add_u32 m0, s20, 0x3000
	s_nop 0
	global_load_lds_dwordx4 v5, s[16:17]
	s_add_u32 m0, s20, 0x4000
	s_nop 0
	global_load_lds_dwordx4 v2, s[18:19]
	s_add_u32 m0, s20, 0x5000
	s_nop 0
	global_load_lds_dwordx4 v3, s[18:19]
	s_add_u32 m0, s20, 0x6000
	s_nop 0
	global_load_lds_dwordx4 v4, s[18:19]
	s_add_u32 m0, s20, 0x7000
	s_nop 0
	global_load_lds_dwordx4 v5, s[18:19]
	s_add_u32 m0, s20, 0x8000
	s_nop 0
	global_load_lds_dwordx4 v6, s[18:19]
	s_add_u32 m0, s20, 0x9000
	s_nop 0
	global_load_lds_dwordx4 v7, s[18:19]
	s_add_u32 s16, s16, 0x80
	s_addc_u32 s17, s17, 0
	s_add_u32 s18, s18, 0x80
	s_addc_u32 s19, s19, 0
	s_add_u32 s20, s20, 0xa000
	s_sub_u32 s22, s20, 0x28000
	s_cmp_ge_u32 s20, 0x28000
	s_cselect_b32 s20, s22, s20
	s_add_u32 m0, s20, 0x0
	s_nop 0
	global_load_lds_dwordx4 v2, s[16:17]
	s_add_u32 m0, s20, 0x1000
	s_nop 0
	global_load_lds_dwordx4 v3, s[16:17]
	s_add_u32 m0, s20, 0x2000
	s_nop 0
	global_load_lds_dwordx4 v4, s[16:17]
	s_add_u32 m0, s20, 0x3000
	s_nop 0
	global_load_lds_dwordx4 v5, s[16:17]
	s_add_u32 m0, s20, 0x4000
	s_nop 0
	global_load_lds_dwordx4 v2, s[18:19]
	v_mov_b32_e32 v64, 0
	v_mov_b32_e32 v65, 0
	v_mov_b32_e32 v66, 0
	v_mov_b32_e32 v67, 0
	v_mov_b32_e32 v68, 0
	v_mov_b32_e32 v69, 0
	v_mov_b32_e32 v70, 0
	v_mov_b32_e32 v71, 0
	v_mov_b32_e32 v72, 0
	v_mov_b32_e32 v73, 0
	v_mov_b32_e32 v74, 0
	v_mov_b32_e32 v75, 0
	v_mov_b32_e32 v76, 0
	v_mov_b32_e32 v77, 0
	v_mov_b32_e32 v78, 0
	v_mov_b32_e32 v79, 0
	v_mov_b32_e32 v80, 0
	v_mov_b32_e32 v81, 0
	v_mov_b32_e32 v82, 0
	v_mov_b32_e32 v83, 0
	v_mov_b32_e32 v84, 0
	v_mov_b32_e32 v85, 0
	v_mov_b32_e32 v86, 0
	v_mov_b32_e32 v87, 0
	v_mov_b32_e32 v88, 0
	v_mov_b32_e32 v89, 0
	v_mov_b32_e32 v90, 0
	v_mov_b32_e32 v91, 0
	v_mov_b32_e32 v92, 0
	v_mov_b32_e32 v93, 0
	v_mov_b32_e32 v94, 0
	v_mov_b32_e32 v95, 0
	v_mov_b32_e32 v96, 0
	v_mov_b32_e32 v97, 0
	v_mov_b32_e32 v98, 0
	v_mov_b32_e32 v99, 0
	v_mov_b32_e32 v100, 0
	v_mov_b32_e32 v101, 0
	v_mov_b32_e32 v102, 0
	v_mov_b32_e32 v103, 0
	v_mov_b32_e32 v104, 0
	v_mov_b32_e32 v105, 0
	v_mov_b32_e32 v106, 0
	v_mov_b32_e32 v107, 0
	v_mov_b32_e32 v108, 0
	v_mov_b32_e32 v109, 0
	v_mov_b32_e32 v110, 0
	v_mov_b32_e32 v111, 0
	v_mov_b32_e32 v112, 0
	v_mov_b32_e32 v113, 0
	v_mov_b32_e32 v114, 0
	v_mov_b32_e32 v115, 0
	v_mov_b32_e32 v116, 0
	v_mov_b32_e32 v117, 0
	v_mov_b32_e32 v118, 0
	v_mov_b32_e32 v119, 0
	v_mov_b32_e32 v120, 0
	v_mov_b32_e32 v121, 0
	v_mov_b32_e32 v122, 0
	v_mov_b32_e32 v123, 0
	v_mov_b32_e32 v124, 0
	v_mov_b32_e32 v125, 0
	v_mov_b32_e32 v126, 0
	v_mov_b32_e32 v127, 0
	v_mov_b32_e32 v128, 0
	v_mov_b32_e32 v129, 0
	v_mov_b32_e32 v130, 0
	v_mov_b32_e32 v131, 0
	v_mov_b32_e32 v132, 0
	v_mov_b32_e32 v133, 0
	v_mov_b32_e32 v134, 0
	v_mov_b32_e32 v135, 0
	v_mov_b32_e32 v136, 0
	v_mov_b32_e32 v137, 0
	v_mov_b32_e32 v138, 0
	v_mov_b32_e32 v139, 0
	v_mov_b32_e32 v140, 0
	v_mov_b32_e32 v141, 0
	v_mov_b32_e32 v142, 0
	v_mov_b32_e32 v143, 0
	v_mov_b32_e32 v144, 0
	v_mov_b32_e32 v145, 0
	v_mov_b32_e32 v146, 0
	v_mov_b32_e32 v147, 0
	v_mov_b32_e32 v148, 0
	v_mov_b32_e32 v149, 0
	v_mov_b32_e32 v150, 0
	v_mov_b32_e32 v151, 0
	v_mov_b32_e32 v152, 0
	v_mov_b32_e32 v153, 0
	v_mov_b32_e32 v154, 0
	v_mov_b32_e32 v155, 0
	v_mov_b32_e32 v156, 0
	v_mov_b32_e32 v157, 0
	v_mov_b32_e32 v158, 0
	v_mov_b32_e32 v159, 0
	s_waitcnt vmcnt(25)
	s_barrier
	v_add_u32_e32 v10, s21, v8
	v_add_u32_e32 v12, s21, v9
	v_xor_b32_e32 v11, 64, v10
	v_xor_b32_e32 v13, 64, v12
	s_add_u32 s21, s21, 0xa000
	s_sub_u32 s23, s21, 0x28000
	s_cmp_ge_u32 s21, 0x28000
	s_cselect_b32 s21, s23, s21
	ds_read_b128 v[160:163], v10 offset:0
	ds_read_b128 v[164:167], v10 offset:2048
	ds_read_b128 v[168:171], v10 offset:4096
	ds_read_b128 v[172:175], v10 offset:6144
	ds_read_b128 v[176:179], v12 offset:0
	ds_read_b128 v[180:183], v12 offset:2048
	ds_read_b128 v[184:187], v12 offset:4096
	ds_read_b128 v[188:191], v12 offset:6144
	ds_read_b128 v[192:195], v12 offset:8192
	ds_read_b128 v[196:199], v12 offset:10240
	s_mov_b32 s15, 0
.Ldn_loop:
	s_waitcnt lgkmcnt(0)
	v_mfma_f32_16x16x32_bf16 v[64:67], v[176:179], v[160:163], v[64:67]
	ds_read_b128 v[200:203], v11 offset:0
	v_mfma_f32_16x16x32_bf16 v[68:71], v[176:179], v[164:167], v[68:71]
	s_add_u32 m0, s20, 0x5000
	v_mfma_f32_16x16x32_bf16 v[72:75], v[176:179], v[168:171], v[72:75]
	ds_read_b128 v[204:207], v11 offset:2048
	v_mfma_f32_16x16x32_bf16 v[76:79], v[176:179], v[172:175], v[76:79]
	global_load_lds_dwordx4 v3, s[18:19]
	v_mfma_f32_16x16x32_bf16 v[80:83], v[180:183], v[160:163], v[80:83]
	ds_read_b128 v[208:211], v11 offset:4096
	v_mfma_f32_16x16x32_bf16 v[84:87], v[180:183], v[164:167], v[84:87]
	s_add_u32 m0, s20, 0x6000
	v_mfma_f32_16x16x32_bf16 v[88:91], v[180:183], v[168:171], v[88:91]
	ds_read_b128 v[212:215], v11 offset:6144
	v_mfma_f32_16x16x32_bf16 v[92:95], v[180:183], v[172:175], v[92:95]
	global_load_lds_dwordx4 v4, s[18:19]
	v_mfma_f32_16x16x32_bf16 v[96:99], v[184:187], v[160:163], v[96:99]
	ds_read_b128 v[216:219], v13 offset:0
	v_mfma_f32_16x16x32_bf16 v[100:103], v[184:187], v[164:167], v[100:103]
	s_add_u32 m0, s20, 0x7000
	v_mfma_f32_16x16x32_bf16 v[104:107], v[184:187], v[168:171], v[104:107]
	ds_read_b128 v[220:223], v13 offset:2048
	v_mfma_f32_16x16x32_bf16 v[108:111], v[184:187], v[172:175], v[108:111]
	global_load_lds_dwordx4 v5, s[18:19]
	v_mfma_f32_16x16x32_bf16 v[112:115], v[188:191], v[160:163], v[112:115]
	ds_read_b128 v[224:227], v13 offset:4096
	v_mfma_f32_16x16x32_bf16 v[116:119], v[188:191], v[164:167], v[116:119]
	s_add_u32 m0, s20, 0x8000
	v_mfma_f32_16x16x32_bf16 v[120:123], v[188:191], v[168:171], v[120:123]
	ds_read_b128 v[228:231], v13 offset:6144
	v_mfma_f32_16x16x32_bf16 v[124:127], v[188:191], v[172:175], v[124:127]
	global_load_lds_dwordx4 v6, s[18:19]
	v_mfma_f32_16x16x32_bf16 v[128:131], v[192:195], v[160:163], v[128:131]
	ds_read_b128 v[232:235], v13 offset:8192
	v_mfma_f32_16x16x32_bf16 v[132:135], v[192:195], v[164:167], v[132:135]
	s_add_u32 m0, s20, 0x9000
	v_mfma_f32_16x16x32_bf16 v[136:139], v[192:195], v[168:171], v[136:139]
	ds_read_b128 v[236:239], v13 offset:10240
	v_mfma_f32_16x16x32_bf16 v[140:143], v[192:195], v[172:175], v[140:143]
	global_load_lds_dwordx4 v7, s[18:19]
	v_mfma_f32_16x16x32_bf16 v[144:147], v[196:199], v[160:163], v[144:147]
	v_mfma_f32_16x16x32_bf16 v[148:151], v[196:199], v[164:167], v[148:151]
	v_mfma_f32_16x16x32_bf16 v[152:155], v[196:199], v[168:171], v[152:155]
	v_mfma_f32_16x16x32_bf16 v[156:159], v[196:199], v[172:175], v[156:159]
	s_add_u32 s16, s16, 0x80
	s_addc_u32 s17, s17, 0
	s_add_u32 s18, s18, 0x80
	s_addc_u32 s19, s19, 0
	s_add_u32 s20, s20, 0xa000
	s_sub_u32 s22, s20, 0x28000
	s_cmp_ge_u32 s20, 0x28000
	s_cselect_b32 s20, s22, s20
	v_add_u32_e32 v10, s21, v8
	v_add_u32_e32 v12, s21, v9
	v_xor_b32_e32 v11, 64, v10
	v_xor_b32_e32 v13, 64, v12
	s_add_u32 s21, s21, 0xa000
	s_sub_u32 s23, s21, 0x28000
	s_cmp_ge_u32 s21, 0x28000
	s_cselect_b32 s21, s23, s21
	s_waitcnt vmcnt(20) lgkmcnt(0)
	s_barrier
	v_mfma_f32_16x16x32_bf16 v[64:67], v[216:219], v[200:203], v[64:67]
	ds_read_b128 v[160:163], v10 offset:0
	v_mfma_f32_16x16x32_bf16 v[68:71], v[216:219], v[204:207], v[68:71]
	s_add_u32 m0, s20, 0x0
	v_mfma_f32_16x16x32_bf16 v[72:75], v[216:219], v[208:211], v[72:75]
	ds_read_b128 v[164:167], v10 offset:2048
	v_mfma_f32_16x16x32_bf16 v[76:79], v[216:219], v[212:215], v[76:79]
	global_load_lds_dwordx4 v2, s[16:17]
	v_mfma_f32_16x16x32_bf16 v[80:83], v[220:223], v[200:203], v[80:83]
	ds_read_b128 v[168:171], v10 offset:4096
	v_mfma_f32_16x16x32_bf16 v[84:87], v[220:223], v[204:207], v[84:87]
	s_add_u32 m0, s20, 0x1000
	v_mfma_f32_16x16x32_bf16 v[88:91], v[220:223], v[208:211], v[88:91]
	ds_read_b128 v[172:175], v10 offset:6144
	v_mfma_f32_16x16x32_bf16 v[92:95], v[220:223], v[212:215], v[92:95]
	global_load_lds_dwordx4 v3, s[16:17]
	v_mfma_f32_16x16x32_bf16 v[96:99], v[224:227], v[200:203], v[96:99]
	ds_read_b128 v[176:179], v12 offset:0
	v_mfma_f32_16x16x32_bf16 v[100:103], v[224:227], v[204:207], v[100:103]
	s_add_u32 m0, s20, 0x2000
	v_mfma_f32_16x16x32_bf16 v[104:107], v[224:227], v[208:211], v[104:107]
	ds_read_b128 v[180:183], v12 offset:2048
	v_mfma_f32_16x16x32_bf16 v[108:111], v[224:227], v[212:215], v[108:111]
	global_load_lds_dwordx4 v4, s[16:17]
	v_mfma_f32_16x16x32_bf16 v[112:115], v[228:231], v[200:203], v[112:115]
	ds_read_b128 v[184:187], v12 offset:4096
	v_mfma_f32_16x16x32_bf16 v[116:119], v[228:231], v[204:207], v[116:119]
	s_add_u32 m0, s20, 0x3000
	v_mfma_f32_16x16x32_bf16 v[120:123], v[228:231], v[208:211], v[120:123]
	ds_read_b128 v[188:191], v12 offset:6144
	v_mfma_f32_16x16x32_bf16 v[124:127], v[228:231], v[212:215], v[124:127]
	global_load_lds_dwordx4 v5, s[16:17]
	v_mfma_f32_16x16x32_bf16 v[128:131], v[232:235], v[200:203], v[128:131]
	ds_read_b128 v[192:195], v12 offset:8192
	v_mfma_f32_16x16x32_bf16 v[132:135], v[232:235], v[204:207], v[132:135]
	s_add_u32 m0, s20, 0x4000
	v_mfma_f32_16x16x32_bf16 v[136:139], v[232:235], v[208:211], v[136:139]
	ds_read_b128 v[196:199], v12 offset:10240
	v_mfma_f32_16x16x32_bf16 v[140:143], v[232:235], v[212:215], v[140:143]
	global_load_lds_dwordx4 v2, s[18:19]
	v_mfma_f32_16x16x32_bf16 v[144:147], v[236:239], v[200:203], v[144:147]
	v_mfma_f32_16x16x32_bf16 v[148:151], v[236:239], v[204:207], v[148:151]
	v_mfma_f32_16x16x32_bf16 v[152:155], v[236:239], v[208:211], v[152:155]
	v_mfma_f32_16x16x32_bf16 v[156:159], v[236:239], v[212:215], v[156:159]
	s_add_u32 s15, s15, 1
	s_cmp_lt_u32 s15, 44
	s_cbranch_scc1 .Ldn_loop
	s_waitcnt lgkmcnt(0)
	v_mfma_f32_16x16x32_bf16 v[64:67], v[176:179], v[160:163], v[64:67]
	ds_read_b128 v[200:203], v11 offset:0
	v_mfma_f32_16x16x32_bf16 v[68:71], v[176:179], v[164:167], v[68:71]
	s_add_u32 m0, s20, 0x5000
	v_mfma_f32_16x16x32_bf16 v[72:75], v[176:179], v[168:171], v[72:75]
	ds_read_b128 v[204:207], v11 offset:2048
	v_mfma_f32_16x16x32_bf16 v[76:79], v[176:179], v[172:175], v[76:79]
	global_load_lds_dwordx4 v3, s[18:19]
	v_mfma_f32_16x16x32_bf16 v[80:83], v[180:183], v[160:163], v[80:83]
	ds_read_b128 v[208:211], v11 offset:4096
	v_mfma_f32_16x16x32_bf16 v[84:87], v[180:183], v[164:167], v[84:87]
	s_add_u32 m0, s20, 0x6000
	v_mfma_f32_16x16x32_bf16 v[88:91], v[180:183], v[168:171], v[88:91]
	ds_read_b128 v[212:215], v11 offset:6144
	v_mfma_f32_16x16x32_bf16 v[92:95], v[180:183], v[172:175], v[92:95]
	global_load_lds_dwordx4 v4, s[18:19]
	v_mfma_f32_16x16x32_bf16 v[96:99], v[184:187], v[160:163], v[96:99]
	ds_read_b128 v[216:219], v13 offset:0
	v_mfma_f32_16x16x32_bf16 v[100:103], v[184:187], v[164:167], v[100:103]
	s_add_u32 m0, s20, 0x7000
	v_mfma_f32_16x16x32_bf16 v[104:107], v[184:187], v[168:171], v[104:107]
	ds_read_b128 v[220:223], v13 offset:2048
	v_mfma_f32_16x16x32_bf16 v[108:111], v[184:187], v[172:175], v[108:111]
	global_load_lds_dwordx4 v5, s[18:19]
	v_mfma_f32_16x16x32_bf16 v[112:115], v[188:191], v[160:163], v[112:115]
	ds_read_b128 v[224:227], v13 offset:4096
	v_mfma_f32_16x16x32_bf16 v[116:119], v[188:191], v[164:167], v[116:119]
	s_add_u32 m0, s20, 0x8000
	v_mfma_f32_16x16x32_bf16 v[120:123], v[188:191], v[168:171], v[120:123]
	ds_read_b128 v[228:231], v13 offset:6144
	v_mfma_f32_16x16x32_bf16 v[124:127], v[188:191], v[172:175], v[124:127]
	global_load_lds_dwordx4 v6, s[18:19]
	v_mfma_f32_16x16x32_bf16 v[128:131], v[192:195], v[160:163], v[128:131]
	ds_read_b128 v[232:235], v13 offset:8192
	v_mfma_f32_16x16x32_bf16 v[132:135], v[192:195], v[164:167], v[132:135]
	s_add_u32 m0, s20, 0x9000
	v_mfma_f32_16x16x32_bf16 v[136:139], v[192:195], v[168:171], v[136:139]
	ds_read_b128 v[236:239], v13 offset:10240
	v_mfma_f32_16x16x32_bf16 v[140:143], v[192:195], v[172:175], v[140:143]
	global_load_lds_dwordx4 v7, s[18:19]
	v_mfma_f32_16x16x32_bf16 v[144:147], v[196:199], v[160:163], v[144:147]
	v_mfma_f32_16x16x32_bf16 v[148:151], v[196:199], v[164:167], v[148:151]
	v_mfma_f32_16x16x32_bf16 v[152:155], v[196:199], v[168:171], v[152:155]
	v_mfma_f32_16x16x32_bf16 v[156:159], v[196:199], v[172:175], v[156:159]
	s_add_u32 s16, s16, 0x80
	s_addc_u32 s17, s17, 0
	s_add_u32 s18, s18, 0x80
	s_addc_u32 s19, s19, 0
	s_add_u32 s20, s20, 0xa000
	s_sub_u32 s22, s20, 0x28000
	s_cmp_ge_u32 s20, 0x28000
	s_cselect_b32 s20, s22, s20
	v_add_u32_e32 v10, s21, v8
	v_add_u32_e32 v12, s21, v9
	v_xor_b32_e32 v11, 64, v10
	v_xor_b32_e32 v13, 64, v12
	s_add_u32 s21, s21, 0xa000
	s_sub_u32 s23, s21, 0x28000
	s_cmp_ge_u32 s21, 0x28000
	s_cselect_b32 s21, s23, s21
	s_waitcnt vmcnt(20) lgkmcnt(0)
	s_barrier
	v_mfma_f32_16x16x32_bf16 v[64:67], v[216:219], v[200:203], v[64:67]
	ds_read_b128 v[160:163], v10 offset:0
	v_mfma_f32_16x16x32_bf16 v[68:71], v[216:219], v[204:207], v[68:71]
	ds_read_b128 v[164:167], v10 offset:2048
	v_mfma_f32_16x16x32_bf16 v[72:75], v[216:219], v[208:211], v[72:75]
	ds_read_b128 v[168:171], v10 offset:4096
	v_mfma_f32_16x16x32_bf16 v[76:79], v[216:219], v[212:215], v[76:79]
	ds_read_b128 v[172:175], v10 offset:6144
	v_mfma_f32_16x16x32_bf16 v[80:83], v[220:223], v[200:203], v[80:83]
	ds_read_b128 v[176:179], v12 offset:0
	v_mfma_f32_16x16x32_bf16 v[84:87], v[220:223], v[204:207], v[84:87]
	ds_read_b128 v[180:183], v12 offset:2048
	v_mfma_f32_16x16x32_bf16 v[88:91], v[220:223], v[208:211], v[88:91]
	ds_read_b128 v[184:187], v12 offset:4096
	v_mfma_f32_16x16x32_bf16 v[92:95], v[220:223], v[212:215], v[92:95]
	ds_read_b128 v[188:191], v12 offset:6144
	v_mfma_f32_16x16x32_bf16 v[96:99], v[224:227], v[200:203], v[96:99]
	ds_read_b128 v[192:195], v12 offset:8192
	v_mfma_f32_16x16x32_bf16 v[100:103], v[224:227], v[204:207], v[100:103]
	ds_read_b128 v[196:199], v12 offset:10240
	v_mfma_f32_16x16x32_bf16 v[104:107], v[224:227], v[208:211], v[104:107]
	v_mfma_f32_16x16x32_bf16 v[108:111], v[224:227], v[212:215], v[108:111]
	v_mfma_f32_16x16x32_bf16 v[112:115], v[228:231], v[200:203], v[112:115]
	v_mfma_f32_16x16x32_bf16 v[116:119], v[228:231], v[204:207], v[116:119]
	v_mfma_f32_16x16x32_bf16 v[120:123], v[228:231], v[208:211], v[120:123]
	v_mfma_f32_16x16x32_bf16 v[124:127], v[228:231], v[212:215], v[124:127]
	v_mfma_f32_16x16x32_bf16 v[128:131], v[232:235], v[200:203], v[128:131]
	v_mfma_f32_16x16x32_bf16 v[132:135], v[232:235], v[204:207], v[132:135]
	v_mfma_f32_16x16x32_bf16 v[136:139], v[232:235], v[208:211], v[136:139]
	v_mfma_f32_16x16x32_bf16 v[140:143], v[232:235], v[212:215], v[140:143]
	v_mfma_f32_16x16x32_bf16 v[144:147], v[236:239], v[200:203], v[144:147]
	v_mfma_f32_16x16x32_bf16 v[148:151], v[236:239], v[204:207], v[148:151]
	v_mfma_f32_16x16x32_bf16 v[152:155], v[236:239], v[208:211], v[152:155]
	v_mfma_f32_16x16x32_bf16 v[156:159], v[236:239], v[212:215], v[156:159]
	s_waitcnt lgkmcnt(0)
	v_mfma_f32_16x16x32_bf16 v[64:67], v[176:179], v[160:163], v[64:67]
	ds_read_b128 v[200:203], v11 offset:0
	v_mfma_f32_16x16x32_bf16 v[68:71], v[176:179], v[164:167], v[68:71]
	ds_read_b128 v[204:207], v11 offset:2048
	v_mfma_f32_16x16x32_bf16 v[72:75], v[176:179], v[168:171], v[72:75]
	ds_read_b128 v[208:211], v11 offset:4096
	v_mfma_f32_16x16x32_bf16 v[76:79], v[176:179], v[172:175], v[76:79]
	ds_read_b128 v[212:215], v11 offset:6144
	v_mfma_f32_16x16x32_bf16 v[80:83], v[180:183], v[160:163], v[80:83]
	ds_read_b128 v[216:219], v13 offset:0
	v_mfma_f32_16x16x32_bf16 v[84:87], v[180:183], v[164:167], v[84:87]
	ds_read_b128 v[220:223], v13 offset:2048
	v_mfma_f32_16x16x32_bf16 v[88:91], v[180:183], v[168:171], v[88:91]
	ds_read_b128 v[224:227], v13 offset:4096
	v_mfma_f32_16x16x32_bf16 v[92:95], v[180:183], v[172:175], v[92:95]
	ds_read_b128 v[228:231], v13 offset:6144
	v_mfma_f32_16x16x32_bf16 v[96:99], v[184:187], v[160:163], v[96:99]
	ds_read_b128 v[232:235], v13 offset:8192
	v_mfma_f32_16x16x32_bf16 v[100:103], v[184:187], v[164:167], v[100:103]
	ds_read_b128 v[236:239], v13 offset:10240
	v_mfma_f32_16x16x32_bf16 v[104:107], v[184:187], v[168:171], v[104:107]
	v_mfma_f32_16x16x32_bf16 v[108:111], v[184:187], v[172:175], v[108:111]
	v_mfma_f32_16x16x32_bf16 v[112:115], v[188:191], v[160:163], v[112:115]
	v_mfma_f32_16x16x32_bf16 v[116:119], v[188:191], v[164:167], v[116:119]
	v_mfma_f32_16x16x32_bf16 v[120:123], v[188:191], v[168:171], v[120:123]
	v_mfma_f32_16x16x32_bf16 v[124:127], v[188:191], v[172:175], v[124:127]
	v_mfma_f32_16x16x32_bf16 v[128:131], v[192:195], v[160:163], v[128:131]
	v_mfma_f32_16x16x32_bf16 v[132:135], v[192:195], v[164:167], v[132:135]
	v_mfma_f32_16x16x32_bf16 v[136:139], v[192:195], v[168:171], v[136:139]
	v_mfma_f32_16x16x32_bf16 v[140:143], v[192:195], v[172:175], v[140:143]
	v_mfma_f32_16x16x32_bf16 v[144:147], v[196:199], v[160:163], v[144:147]
	v_mfma_f32_16x16x32_bf16 v[148:151], v[196:199], v[164:167], v[148:151]
	v_mfma_f32_16x16x32_bf16 v[152:155], v[196:199], v[168:171], v[152:155]
	v_mfma_f32_16x16x32_bf16 v[156:159], v[196:199], v[172:175], v[156:159]
	v_add_u32_e32 v10, s21, v8
	v_add_u32_e32 v12, s21, v9
	v_xor_b32_e32 v11, 64, v10
	v_xor_b32_e32 v13, 64, v12
	s_add_u32 s21, s21, 0xa000
	s_sub_u32 s23, s21, 0x28000
	s_cmp_ge_u32 s21, 0x28000
	s_cselect_b32 s21, s23, s21
	s_waitcnt vmcnt(10) lgkmcnt(0)
	s_barrier
	v_mfma_f32_16x16x32_bf16 v[64:67], v[216:219], v[200:203], v[64:67]
	ds_read_b128 v[160:163], v10 offset:0
	v_mfma_f32_16x16x32_bf16 v[68:71], v[216:219], v[204:207], v[68:71]
	ds_read_b128 v[164:167], v10 offset:2048
	v_mfma_f32_16x16x32_bf16 v[72:75], v[216:219], v[208:211], v[72:75]
	ds_read_b128 v[168:171], v10 offset:4096
	v_mfma_f32_16x16x32_bf16 v[76:79], v[216:219], v[212:215], v[76:79]
	ds_read_b128 v[172:175], v10 offset:6144
	v_mfma_f32_16x16x32_bf16 v[80:83], v[220:223], v[200:203], v[80:83]
	ds_read_b128 v[176:179], v12 offset:0
	v_mfma_f32_16x16x32_bf16 v[84:87], v[220:223], v[204:207], v[84:87]
	ds_read_b128 v[180:183], v12 offset:2048
	v_mfma_f32_16x16x32_bf16 v[88:91], v[220:223], v[208:211], v[88:91]
	ds_read_b128 v[184:187], v12 offset:4096
	v_mfma_f32_16x16x32_bf16 v[92:95], v[220:223], v[212:215], v[92:95]
	ds_read_b128 v[188:191], v12 offset:6144
	v_mfma_f32_16x16x32_bf16 v[96:99], v[224:227], v[200:203], v[96:99]
	ds_read_b128 v[192:195], v12 offset:8192
	v_mfma_f32_16x16x32_bf16 v[100:103], v[224:227], v[204:207], v[100:103]
	ds_read_b128 v[196:199], v12 offset:10240
	v_mfma_f32_16x16x32_bf16 v[104:107], v[224:227], v[208:211], v[104:107]
	v_mfma_f32_16x16x32_bf16 v[108:111], v[224:227], v[212:215], v[108:111]
	v_mfma_f32_16x16x32_bf16 v[112:115], v[228:231], v[200:203], v[112:115]
	v_mfma_f32_16x16x32_bf16 v[116:119], v[228:231], v[204:207], v[116:119]
	v_mfma_f32_16x16x32_bf16 v[120:123], v[228:231], v[208:211], v[120:123]
	v_mfma_f32_16x16x32_bf16 v[124:127], v[228:231], v[212:215], v[124:127]
	v_mfma_f32_16x16x32_bf16 v[128:131], v[232:235], v[200:203], v[128:131]
	v_mfma_f32_16x16x32_bf16 v[132:135], v[232:235], v[204:207], v[132:135]
	v_mfma_f32_16x16x32_bf16 v[136:139], v[232:235], v[208:211], v[136:139]
	v_mfma_f32_16x16x32_bf16 v[140:143], v[232:235], v[212:215], v[140:143]
	v_mfma_f32_16x16x32_bf16 v[144:147], v[236:239], v[200:203], v[144:147]
	v_mfma_f32_16x16x32_bf16 v[148:151], v[236:239], v[204:207], v[148:151]
	v_mfma_f32_16x16x32_bf16 v[152:155], v[236:239], v[208:211], v[152:155]
	v_mfma_f32_16x16x32_bf16 v[156:159], v[236:239], v[212:215], v[156:159]
	s_waitcnt lgkmcnt(0)
	v_mfma_f32_16x16x32_bf16 v[64:67], v[176:179], v[160:163], v[64:67]
	ds_read_b128 v[200:203], v11 offset:0
	v_mfma_f32_16x16x32_bf16 v[68:71], v[176:179], v[164:167], v[68:71]
	ds_read_b128 v[204:207], v11 offset:2048
	v_mfma_f32_16x16x32_bf16 v[72:75], v[176:179], v[168:171], v[72:75]
	ds_read_b128 v[208:211], v11 offset:4096
	v_mfma_f32_16x16x32_bf16 v[76:79], v[176:179], v[172:175], v[76:79]
	ds_read_b128 v[212:215], v11 offset:6144
	v_mfma_f32_16x16x32_bf16 v[80:83], v[180:183], v[160:163], v[80:83]
	ds_read_b128 v[216:219], v13 offset:0
	v_mfma_f32_16x16x32_bf16 v[84:87], v[180:183], v[164:167], v[84:87]
	ds_read_b128 v[220:223], v13 offset:2048
	v_mfma_f32_16x16x32_bf16 v[88:91], v[180:183], v[168:171], v[88:91]
	ds_read_b128 v[224:227], v13 offset:4096
	v_mfma_f32_16x16x32_bf16 v[92:95], v[180:183], v[172:175], v[92:95]
	ds_read_b128 v[228:231], v13 offset:6144
	v_mfma_f32_16x16x32_bf16 v[96:99], v[184:187], v[160:163], v[96:99]
	ds_read_b128 v[232:235], v13 offset:8192
	v_mfma_f32_16x16x32_bf16 v[100:103], v[184:187], v[164:167], v[100:103]
	ds_read_b128 v[236:239], v13 offset:10240
	v_mfma_f32_16x16x32_bf16 v[104:107], v[184:187], v[168:171], v[104:107]
	v_mfma_f32_16x16x32_bf16 v[108:111], v[184:187], v[172:175], v[108:111]
	v_mfma_f32_16x16x32_bf16 v[112:115], v[188:191], v[160:163], v[112:115]
	v_mfma_f32_16x16x32_bf16 v[116:119], v[188:191], v[164:167], v[116:119]
	v_mfma_f32_16x16x32_bf16 v[120:123], v[188:191], v[168:171], v[120:123]
	v_mfma_f32_16x16x32_bf16 v[124:127], v[188:191], v[172:175], v[124:127]
	v_mfma_f32_16x16x32_bf16 v[128:131], v[192:195], v[160:163], v[128:131]
	v_mfma_f32_16x16x32_bf16 v[132:135], v[192:195], v[164:167], v[132:135]
	v_mfma_f32_16x16x32_bf16 v[136:139], v[192:195], v[168:171], v[136:139]
	v_mfma_f32_16x16x32_bf16 v[140:143], v[192:195], v[172:175], v[140:143]
	v_mfma_f32_16x16x32_bf16 v[144:147], v[196:199], v[160:163], v[144:147]
	v_mfma_f32_16x16x32_bf16 v[148:151], v[196:199], v[164:167], v[148:151]
	v_mfma_f32_16x16x32_bf16 v[152:155], v[196:199], v[168:171], v[152:155]
	v_mfma_f32_16x16x32_bf16 v[156:159], v[196:199], v[172:175], v[156:159]
	v_add_u32_e32 v10, s21, v8
	v_add_u32_e32 v12, s21, v9
	v_xor_b32_e32 v11, 64, v10
	v_xor_b32_e32 v13, 64, v12
	s_add_u32 s21, s21, 0xa000
	s_sub_u32 s23, s21, 0x28000
	s_cmp_ge_u32 s21, 0x28000
	s_cselect_b32 s21, s23, s21
	s_waitcnt vmcnt(0) lgkmcnt(0)
	s_barrier
	v_mfma_f32_16x16x32_bf16 v[64:67], v[216:219], v[200:203], v[64:67]
	ds_read_b128 v[160:163], v10 offset:0
	v_mfma_f32_16x16x32_bf16 v[68:71], v[216:219], v[204:207], v[68:71]
	global_load_dwordx4 v[16:19], v56, s[8:9] offset:0
	v_mfma_f32_16x16x32_bf16 v[72:75], v[216:219], v[208:211], v[72:75]
	ds_read_b128 v[164:167], v10 offset:2048
	v_mfma_f32_16x16x32_bf16 v[76:79], v[216:219], v[212:215], v[76:79]
	global_load_dwordx4 v[20:23], v57, s[8:9] offset:0
	v_mfma_f32_16x16x32_bf16 v[80:83], v[220:223], v[200:203], v[80:83]
	ds_read_b128 v[168:171], v10 offset:4096
	v_mfma_f32_16x16x32_bf16 v[84:87], v[220:223], v[204:207], v[84:87]
	global_load_dwordx4 v[24:27], v58, s[8:9] offset:0
	v_mfma_f32_16x16x32_bf16 v[88:91], v[220:223], v[208:211], v[88:91]
	ds_read_b128 v[172:175], v10 offset:6144
	v_mfma_f32_16x16x32_bf16 v[92:95], v[220:223], v[212:215], v[92:95]
	global_load_dwordx4 v[28:31], v59, s[8:9] offset:0
	v_mfma_f32_16x16x32_bf16 v[96:99], v[224:227], v[200:203], v[96:99]
	ds_read_b128 v[176:179], v12 offset:0
	v_mfma_f32_16x16x32_bf16 v[100:103], v[224:227], v[204:207], v[100:103]
	global_load_dwordx4 v[32:35], v56, s[8:9] offset:64
	v_mfma_f32_16x16x32_bf16 v[104:107], v[224:227], v[208:211], v[104:107]
	ds_read_b128 v[180:183], v12 offset:2048
	v_mfma_f32_16x16x32_bf16 v[108:111], v[224:227], v[212:215], v[108:111]
	global_load_dwordx4 v[36:39], v57, s[8:9] offset:64
	v_mfma_f32_16x16x32_bf16 v[112:115], v[228:231], v[200:203], v[112:115]
	ds_read_b128 v[184:187], v12 offset:4096
	v_mfma_f32_16x16x32_bf16 v[116:119], v[228:231], v[204:207], v[116:119]
	global_load_dwordx4 v[40:43], v58, s[8:9] offset:64
	v_mfma_f32_16x16x32_bf16 v[120:123], v[228:231], v[208:211], v[120:123]
	ds_read_b128 v[188:191], v12 offset:6144
	v_mfma_f32_16x16x32_bf16 v[124:127], v[228:231], v[212:215], v[124:127]
	global_load_dwordx4 v[44:47], v59, s[8:9] offset:64
	v_mfma_f32_16x16x32_bf16 v[128:131], v[232:235], v[200:203], v[128:131]
	ds_read_b128 v[192:195], v12 offset:8192
	v_mfma_f32_16x16x32_bf16 v[132:135], v[232:235], v[204:207], v[132:135]
	global_load_dwordx4 v[48:51], v56, s[8:9] offset:128
	v_mfma_f32_16x16x32_bf16 v[136:139], v[232:235], v[208:211], v[136:139]
	ds_read_b128 v[196:199], v12 offset:10240
	v_mfma_f32_16x16x32_bf16 v[140:143], v[232:235], v[212:215], v[140:143]
	global_load_dwordx4 v[52:55], v57, s[8:9] offset:128
	v_mfma_f32_16x16x32_bf16 v[144:147], v[236:239], v[200:203], v[144:147]
	global_load_dwordx4 v[240:243], v58, s[8:9] offset:128
	v_mfma_f32_16x16x32_bf16 v[148:151], v[236:239], v[204:207], v[148:151]
	global_load_dwordx4 v[244:247], v59, s[8:9] offset:128
	v_mfma_f32_16x16x32_bf16 v[152:155], v[236:239], v[208:211], v[152:155]
	global_load_dwordx4 v[248:251], v56, s[8:9] offset:192
	v_mfma_f32_16x16x32_bf16 v[156:159], v[236:239], v[212:215], v[156:159]
	global_load_dwordx4 v[252:255], v57, s[8:9] offset:192
	s_waitcnt lgkmcnt(0)
	v_mfma_f32_16x16x32_bf16 v[64:67], v[176:179], v[160:163], v[64:67]
	ds_read_b128 v[200:203], v11 offset:0
	v_mfma_f32_16x16x32_bf16 v[68:71], v[176:179], v[164:167], v[68:71]
	ds_read_b128 v[204:207], v11 offset:2048
	v_mfma_f32_16x16x32_bf16 v[72:75], v[176:179], v[168:171], v[72:75]
	ds_read_b128 v[208:211], v11 offset:4096
	v_mfma_f32_16x16x32_bf16 v[76:79], v[176:179], v[172:175], v[76:79]
	ds_read_b128 v[212:215], v11 offset:6144
	v_mfma_f32_16x16x32_bf16 v[80:83], v[180:183], v[160:163], v[80:83]
	ds_read_b128 v[216:219], v13 offset:0
	v_mfma_f32_16x16x32_bf16 v[84:87], v[180:183], v[164:167], v[84:87]
	ds_read_b128 v[220:223], v13 offset:2048
	v_mfma_f32_16x16x32_bf16 v[88:91], v[180:183], v[168:171], v[88:91]
	ds_read_b128 v[224:227], v13 offset:4096
	v_mfma_f32_16x16x32_bf16 v[92:95], v[180:183], v[172:175], v[92:95]
	ds_read_b128 v[228:231], v13 offset:6144
	v_mfma_f32_16x16x32_bf16 v[96:99], v[184:187], v[160:163], v[96:99]
	ds_read_b128 v[232:235], v13 offset:8192
	v_mfma_f32_16x16x32_bf16 v[100:103], v[184:187], v[164:167], v[100:103]
	ds_read_b128 v[236:239], v13 offset:10240
	v_mfma_f32_16x16x32_bf16 v[104:107], v[184:187], v[168:171], v[104:107]
	v_mfma_f32_16x16x32_bf16 v[108:111], v[184:187], v[172:175], v[108:111]
	v_mfma_f32_16x16x32_bf16 v[112:115], v[188:191], v[160:163], v[112:115]
	v_mfma_f32_16x16x32_bf16 v[116:119], v[188:191], v[164:167], v[116:119]
	v_mfma_f32_16x16x32_bf16 v[120:123], v[188:191], v[168:171], v[120:123]
	v_mfma_f32_16x16x32_bf16 v[124:127], v[188:191], v[172:175], v[124:127]
	v_mfma_f32_16x16x32_bf16 v[128:131], v[192:195], v[160:163], v[128:131]
	v_mfma_f32_16x16x32_bf16 v[132:135], v[192:195], v[164:167], v[132:135]
	v_mfma_f32_16x16x32_bf16 v[136:139], v[192:195], v[168:171], v[136:139]
	v_mfma_f32_16x16x32_bf16 v[140:143], v[192:195], v[172:175], v[140:143]
	v_mfma_f32_16x16x32_bf16 v[144:147], v[196:199], v[160:163], v[144:147]
	v_mfma_f32_16x16x32_bf16 v[148:151], v[196:199], v[164:167], v[148:151]
	v_mfma_f32_16x16x32_bf16 v[152:155], v[196:199], v[168:171], v[152:155]
	v_mfma_f32_16x16x32_bf16 v[156:159], v[196:199], v[172:175], v[156:159]
	s_waitcnt lgkmcnt(0)
	v_mfma_f32_16x16x32_bf16 v[64:67], v[216:219], v[200:203], v[64:67]
	v_mfma_f32_16x16x32_bf16 v[68:71], v[216:219], v[204:207], v[68:71]
	global_load_dwordx4 v[160:163], v58, s[8:9] offset:192
	v_mfma_f32_16x16x32_bf16 v[72:75], v[216:219], v[208:211], v[72:75]
	v_mfma_f32_16x16x32_bf16 v[76:79], v[216:219], v[212:215], v[76:79]
	global_load_dwordx4 v[164:167], v59, s[8:9] offset:192
	v_mfma_f32_16x16x32_bf16 v[80:83], v[220:223], v[200:203], v[80:83]
	v_mfma_f32_16x16x32_bf16 v[84:87], v[220:223], v[204:207], v[84:87]
	global_load_dwordx4 v[168:171], v56, s[8:9] offset:256
	v_mfma_f32_16x16x32_bf16 v[88:91], v[220:223], v[208:211], v[88:91]
	v_mfma_f32_16x16x32_bf16 v[92:95], v[220:223], v[212:215], v[92:95]
	global_load_dwordx4 v[172:175], v57, s[8:9] offset:256
	v_mfma_f32_16x16x32_bf16 v[96:99], v[224:227], v[200:203], v[96:99]
	v_mfma_f32_16x16x32_bf16 v[100:103], v[224:227], v[204:207], v[100:103]
	global_load_dwordx4 v[176:179], v58, s[8:9] offset:256
	v_mfma_f32_16x16x32_bf16 v[104:107], v[224:227], v[208:211], v[104:107]
	v_mfma_f32_16x16x32_bf16 v[108:111], v[224:227], v[212:215], v[108:111]
	global_load_dwordx4 v[180:183], v59, s[8:9] offset:256
	v_mfma_f32_16x16x32_bf16 v[112:115], v[228:231], v[200:203], v[112:115]
	v_mfma_f32_16x16x32_bf16 v[116:119], v[228:231], v[204:207], v[116:119]
	global_load_dwordx4 v[184:187], v56, s[8:9] offset:320
	v_mfma_f32_16x16x32_bf16 v[120:123], v[228:231], v[208:211], v[120:123]
	v_mfma_f32_16x16x32_bf16 v[124:127], v[228:231], v[212:215], v[124:127]
	global_load_dwordx4 v[188:191], v57, s[8:9] offset:320
	v_mfma_f32_16x16x32_bf16 v[128:131], v[232:235], v[200:203], v[128:131]
	v_mfma_f32_16x16x32_bf16 v[132:135], v[232:235], v[204:207], v[132:135]
	global_load_dwordx4 v[192:195], v58, s[8:9] offset:320
	v_mfma_f32_16x16x32_bf16 v[136:139], v[232:235], v[208:211], v[136:139]
	v_mfma_f32_16x16x32_bf16 v[140:143], v[232:235], v[212:215], v[140:143]
	global_load_dwordx4 v[196:199], v59, s[8:9] offset:320
	v_mfma_f32_16x16x32_bf16 v[144:147], v[236:239], v[200:203], v[144:147]
	v_mfma_f32_16x16x32_bf16 v[148:151], v[236:239], v[204:207], v[148:151]
	v_mfma_f32_16x16x32_bf16 v[152:155], v[236:239], v[208:211], v[152:155]
	v_mfma_f32_16x16x32_bf16 v[156:159], v[236:239], v[212:215], v[156:159]
	s_waitcnt vmcnt(23)
	v_pk_add_f32 v[64:65], v[64:65], v[16:17]
	v_pk_add_f32 v[66:67], v[66:67], v[18:19]
	global_store_dwordx4 v56, v[64:67], s[10:11] offset:0
	s_waitcnt vmcnt(23)
	v_pk_add_f32 v[68:69], v[68:69], v[20:21]
	v_pk_add_f32 v[70:71], v[70:71], v[22:23]
	global_store_dwordx4 v57, v[68:71], s[10:11] offset:0
	s_waitcnt vmcnt(23)
	v_pk_add_f32 v[72:73], v[72:73], v[24:25]
	v_pk_add_f32 v[74:75], v[74:75], v[26:27]
	global_store_dwordx4 v58, v[72:75], s[10:11] offset:0
	s_waitcnt vmcnt(23)
	v_pk_add_f32 v[76:77], v[76:77], v[28:29]
	v_pk_add_f32 v[78:79], v[78:79], v[30:31]
	global_store_dwordx4 v59, v[76:79], s[10:11] offset:0
	s_waitcnt vmcnt(23)
	v_pk_add_f32 v[80:81], v[80:81], v[32:33]
	v_pk_add_f32 v[82:83], v[82:83], v[34:35]
	global_store_dwordx4 v56, v[80:83], s[10:11] offset:64
	s_waitcnt vmcnt(23)
	v_pk_add_f32 v[84:85], v[84:85], v[36:37]
	v_pk_add_f32 v[86:87], v[86:87], v[38:39]
	global_store_dwordx4 v57, v[84:87], s[10:11] offset:64
	s_waitcnt vmcnt(23)
	v_pk_add_f32 v[88:89], v[88:89], v[40:41]
	v_pk_add_f32 v[90:91], v[90:91], v[42:43]
	global_store_dwordx4 v58, v[88:91], s[10:11] offset:64
	s_waitcnt vmcnt(23)
	v_pk_add_f32 v[92:93], v[92:93], v[44:45]
	v_pk_add_f32 v[94:95], v[94:95], v[46:47]
	global_store_dwordx4 v59, v[92:95], s[10:11] offset:64
	s_waitcnt vmcnt(23)
	v_pk_add_f32 v[96:97], v[96:97], v[48:49]
	v_pk_add_f32 v[98:99], v[98:99], v[50:51]
	global_store_dwordx4 v56, v[96:99], s[10:11] offset:128
	s_waitcnt vmcnt(23)
	v_pk_add_f32 v[100:101], v[100:101], v[52:53]
	v_pk_add_f32 v[102:103], v[102:103], v[54:55]
	global_store_dwordx4 v57, v[100:103], s[10:11] offset:128
	s_waitcnt vmcnt(23)
	v_pk_add_f32 v[104:105], v[104:105], v[240:241]
	v_pk_add_f32 v[106:107], v[106:107], v[242:243]
	global_store_dwordx4 v58, v[104:107], s[10:11] offset:128
	s_waitcnt vmcnt(23)
	v_pk_add_f32 v[108:109], v[108:109], v[244:245]
	v_pk_add_f32 v[110:111], v[110:111], v[246:247]
	global_store_dwordx4 v59, v[108:111], s[10:11] offset:128
	s_waitcnt vmcnt(23)
	v_pk_add_f32 v[112:113], v[112:113], v[248:249]
	v_pk_add_f32 v[114:115], v[114:115], v[250:251]
	global_store_dwordx4 v56, v[112:115], s[10:11] offset:192
	s_waitcnt vmcnt(23)
	v_pk_add_f32 v[116:117], v[116:117], v[252:253]
	v_pk_add_f32 v[118:119], v[118:119], v[254:255]
	global_store_dwordx4 v57, v[116:119], s[10:11] offset:192
	s_waitcnt vmcnt(23)
	v_pk_add_f32 v[120:121], v[120:121], v[160:161]
	v_pk_add_f32 v[122:123], v[122:123], v[162:163]
	global_store_dwordx4 v58, v[120:123], s[10:11] offset:192
	s_waitcnt vmcnt(23)
	v_pk_add_f32 v[124:125], v[124:125], v[164:165]
	v_pk_add_f32 v[126:127], v[126:127], v[166:167]
	global_store_dwordx4 v59, v[124:127], s[10:11] offset:192
	s_waitcnt vmcnt(23)
	v_pk_add_f32 v[128:129], v[128:129], v[168:169]
	v_pk_add_f32 v[130:131], v[130:131], v[170:171]
	global_store_dwordx4 v56, v[128:131], s[10:11] offset:256
	s_waitcnt vmcnt(23)
	v_pk_add_f32 v[132:133], v[132:133], v[172:173]
	v_pk_add_f32 v[134:135], v[134:135], v[174:175]
	global_store_dwordx4 v57, v[132:135], s[10:11] offset:256
	s_waitcnt vmcnt(23)
	v_pk_add_f32 v[136:137], v[136:137], v[176:177]
	v_pk_add_f32 v[138:139], v[138:139], v[178:179]
	global_store_dwordx4 v58, v[136:139], s[10:11] offset:256
	s_waitcnt vmcnt(23)
	v_pk_add_f32 v[140:141], v[140:141], v[180:181]
	v_pk_add_f32 v[142:143], v[142:143], v[182:183]
	global_store_dwordx4 v59, v[140:143], s[10:11] offset:256
	s_waitcnt vmcnt(23)
	v_pk_add_f32 v[144:145], v[144:145], v[184:185]
	v_pk_add_f32 v[146:147], v[146:147], v[186:187]
	global_store_dwordx4 v56, v[144:147], s[10:11] offset:320
	s_waitcnt vmcnt(23)
	v_pk_add_f32 v[148:149], v[148:149], v[188:189]
	v_pk_add_f32 v[150:151], v[150:151], v[190:191]
	global_store_dwordx4 v57, v[148:151], s[10:11] offset:320
	s_waitcnt vmcnt(23)
	v_pk_add_f32 v[152:153], v[152:153], v[192:193]
	v_pk_add_f32 v[154:155], v[154:155], v[194:195]
	global_store_dwordx4 v58, v[152:155], s[10:11] offset:320
	s_waitcnt vmcnt(23)
	v_pk_add_f32 v[156:157], v[156:157], v[196:197]
	v_pk_add_f32 v[158:159], v[158:159], v[198:199]
	global_store_dwordx4 v59, v[156:159], s[10:11] offset:320
